# odd in-proj GEMM epilogue stores written through (sc1) so the barrier write-back finds less dirty data
# baseline (speedup 1.0000x reference)
.LBB0_1610:
	v_readlane_b32 s16, v252, 13
	v_lshl_add_u32 v158, s37, 8, v146
	v_lshl_or_b32 v152, s41, 8, v148
	v_readlane_b32 s17, v252, 14
	v_ashrrev_i32_e32 v153, 31, v152
	v_cvt_pk_bf16_f32 v118, v118, v119
	v_mov_b64_e32 v[154:155], s[16:17]
	v_cvt_pk_bf16_f32 v119, v120, v121
	v_cvt_pk_bf16_f32 v120, v114, v115
	v_or_b32_e32 v114, 16, v158
	v_cvt_pk_bf16_f32 v102, v102, v103
	v_cvt_pk_bf16_f32 v103, v104, v105
	v_cvt_pk_bf16_f32 v104, v98, v99
	v_or_b32_e32 v98, 32, v158
	v_cvt_pk_bf16_f32 v86, v86, v87
	v_cvt_pk_bf16_f32 v87, v88, v89
	v_cvt_pk_bf16_f32 v88, v82, v83
	v_or_b32_e32 v82, 48, v158
	v_cvt_pk_bf16_f32 v70, v70, v71
	v_cvt_pk_bf16_f32 v71, v72, v73
	v_cvt_pk_bf16_f32 v72, v66, v67
	v_add_u32_e32 v66, 0x80, v158
	v_cvt_pk_bf16_f32 v54, v54, v55
	v_cvt_pk_bf16_f32 v55, v56, v57
	v_cvt_pk_bf16_f32 v56, v50, v51
	v_add_u32_e32 v50, 0x90, v158
	v_cvt_pk_bf16_f32 v38, v38, v39
	v_cvt_pk_bf16_f32 v39, v40, v41
	v_cvt_pk_bf16_f32 v40, v34, v35
	v_add_u32_e32 v34, 0xa0, v158
	v_cvt_pk_bf16_f32 v22, v22, v23
	v_cvt_pk_bf16_f32 v23, v24, v25
	v_cvt_pk_bf16_f32 v24, v18, v19
	v_add_u32_e32 v18, 0xb0, v158
	v_mad_i64_i32 v[156:157], s[16:17], v158, s44, v[154:155]
	v_lshlrev_b64 v[152:153], 1, v[152:153]
	v_mad_i64_i32 v[114:115], s[16:17], v114, s44, v[154:155]
	v_mad_i64_i32 v[98:99], s[16:17], v98, s44, v[154:155]
	v_mad_i64_i32 v[82:83], s[16:17], v82, s44, v[154:155]
	v_mad_i64_i32 v[66:67], s[16:17], v66, s44, v[154:155]
	v_mad_i64_i32 v[50:51], s[16:17], v50, s44, v[154:155]
	v_mad_i64_i32 v[34:35], s[16:17], v34, s44, v[154:155]
	v_mad_i64_i32 v[18:19], s[16:17], v18, s44, v[154:155]
	v_lshl_add_u64 v[156:157], v[156:157], 0, v[152:153]
	v_cvt_pk_bf16_f32 v126, v126, v127
	v_cvt_pk_bf16_f32 v127, v128, v129
	v_cvt_pk_bf16_f32 v128, v122, v123
	v_cvt_pk_bf16_f32 v129, v124, v125
	v_cvt_pk_bf16_f32 v121, v116, v117
	v_lshl_add_u64 v[114:115], v[114:115], 0, v[152:153]
	v_cvt_pk_bf16_f32 v110, v110, v111
	v_cvt_pk_bf16_f32 v111, v112, v113
	v_cvt_pk_bf16_f32 v112, v106, v107
	v_cvt_pk_bf16_f32 v113, v108, v109
	v_cvt_pk_bf16_f32 v105, v100, v101
	v_lshl_add_u64 v[98:99], v[98:99], 0, v[152:153]
	v_cvt_pk_bf16_f32 v94, v94, v95
	v_cvt_pk_bf16_f32 v95, v96, v97
	v_cvt_pk_bf16_f32 v96, v90, v91
	v_cvt_pk_bf16_f32 v97, v92, v93
	v_cvt_pk_bf16_f32 v89, v84, v85
	v_lshl_add_u64 v[82:83], v[82:83], 0, v[152:153]
	v_cvt_pk_bf16_f32 v78, v78, v79
	v_cvt_pk_bf16_f32 v79, v80, v81
	v_cvt_pk_bf16_f32 v80, v74, v75
	v_cvt_pk_bf16_f32 v81, v76, v77
	v_cvt_pk_bf16_f32 v73, v68, v69
	v_lshl_add_u64 v[66:67], v[66:67], 0, v[152:153]
	v_cvt_pk_bf16_f32 v62, v62, v63
	v_cvt_pk_bf16_f32 v63, v64, v65
	v_cvt_pk_bf16_f32 v64, v58, v59
	v_cvt_pk_bf16_f32 v65, v60, v61
	v_cvt_pk_bf16_f32 v57, v52, v53
	v_lshl_add_u64 v[50:51], v[50:51], 0, v[152:153]
	v_cvt_pk_bf16_f32 v46, v46, v47
	v_cvt_pk_bf16_f32 v47, v48, v49
	v_cvt_pk_bf16_f32 v48, v42, v43
	v_cvt_pk_bf16_f32 v49, v44, v45
	v_cvt_pk_bf16_f32 v41, v36, v37
	v_lshl_add_u64 v[34:35], v[34:35], 0, v[152:153]
	v_cvt_pk_bf16_f32 v30, v30, v31
	v_cvt_pk_bf16_f32 v31, v32, v33
	v_cvt_pk_bf16_f32 v32, v26, v27
	v_cvt_pk_bf16_f32 v33, v28, v29
	v_cvt_pk_bf16_f32 v25, v20, v21
	v_lshl_add_u64 v[18:19], v[18:19], 0, v[152:153]
	v_cvt_pk_bf16_f32 v14, v14, v15
	v_cvt_pk_bf16_f32 v15, v16, v17
	v_cvt_pk_bf16_f32 v16, v10, v11
	v_cvt_pk_bf16_f32 v17, v12, v13
	v_cvt_pk_bf16_f32 v6, v6, v7
	v_cvt_pk_bf16_f32 v7, v8, v9
	v_cvt_pk_bf16_f32 v8, v2, v3
	v_cvt_pk_bf16_f32 v9, v4, v5
	s_and_b64 vcc, exec, s[4:5]
	s_mov_b32 s41, s45
	s_mov_b32 s37, s46
	s_mov_b64 s[18:19], s[8:9]
	s_mov_b64 s[16:17], s[6:7]
	global_store_dwordx4 v[156:157], v[126:129], off sc1
	global_store_dwordx4 v[156:157], v[118:121], off offset:256 sc1
	global_store_dwordx4 v[114:115], v[110:113], off sc1
	global_store_dwordx4 v[114:115], v[102:105], off offset:256 sc1
	global_store_dwordx4 v[98:99], v[94:97], off sc1
	global_store_dwordx4 v[98:99], v[86:89], off offset:256 sc1
	global_store_dwordx4 v[82:83], v[78:81], off sc1
	global_store_dwordx4 v[82:83], v[70:73], off offset:256 sc1
	global_store_dwordx4 v[66:67], v[62:65], off sc1
	global_store_dwordx4 v[66:67], v[54:57], off offset:256 sc1
	global_store_dwordx4 v[50:51], v[46:49], off sc1
	global_store_dwordx4 v[50:51], v[38:41], off offset:256 sc1
	global_store_dwordx4 v[34:35], v[30:33], off sc1
	global_store_dwordx4 v[34:35], v[22:25], off offset:256 sc1
	global_store_dwordx4 v[18:19], v[14:17], off sc1
	global_store_dwordx4 v[18:19], v[6:9], off offset:256 sc1
	s_cbranch_vccnz .LBB0_1621
